# moe combine: residual-stream x loads (read last) and stores (next read 13 phases later) marked nt
# baseline (speedup 1.0000x reference)
; DI float bflo(unsigned w) { return __uint_as_float(w << 16); }
; DI float bfhi(unsigned w) { return __uint_as_float(w & 0xffff0000u); }
;     DI float* outp() const { return (float*)out_g; }
;     ...
;     for (int tb = gw * 4; tb < T; tb += NGW * 4) {
;         int tbase = tb; asm volatile("" : "+s"(tbase), "+v"(lane));
;         int r0[4], r1[4];
; #pragma unroll
;         for (int e = 0; e < 4; ++e) { r0[e] = ROW[(tbase + e) * 2]; r1[e] = ROW[(tbase + e) * 2 + 1]; }
;         u32x2 ya[4][4], yb[4][4]; f32x4 xv[4][4];
; #pragma unroll
;         for (int e = 0; e < 4; ++e) { const u32x2* y0 = (const u32x2*)(YE + (size_t)r0[e] * DM) + lane; const u32x2* y1 = (const u32x2*)(YE + (size_t)r1[e] * DM) + lane; const f32x4* xr = (const f32x4*)(F.outp() + (size_t)(tbase + e) * DM) + lane;
; #pragma unroll
;             for (int j = 0; j < 4; ++j) { ya[e][j] = __builtin_nontemporal_load(y0 + 64 * j); yb[e][j] = __builtin_nontemporal_load(y1 + 64 * j); xv[e][j] = xr[64 * j]; } }
; #pragma unroll
;         for (int e = 0; e < 4; ++e) { const int t = tbase + e; f32x4* xr = (f32x4*)(xout + (size_t)t * DM) + lane; float s = 0.f;
; #pragma unroll
;             for (int j = 0; j < 4; ++j) { f32x4 v = xv[e][j]; const u32x2 a = ya[e][j], b = yb[e][j];
;                 v.x += bflo(a.x) + bflo(b.x); v.y += bfhi(a.x) + bfhi(b.x); v.z += bflo(a.y) + bflo(b.y); v.w += bfhi(a.y) + bfhi(b.y);
.LBB0_3079:
	s_mov_b32 s12, s22
	s_lshl_b32 s4, s12, 1
	s_ashr_i32 s5, s4, 31
	s_lshl_b64 s[4:5], s[4:5], 2
	s_add_u32 s20, s23, s4
	s_addc_u32 s21, s24, s5
	global_load_dwordx2 v[16:17], v65, s[20:21]
	s_add_i32 s10, s12, 1
	s_lshl_b32 s4, s10, 1
	s_ashr_i32 s5, s4, 31
	s_lshl_b64 s[4:5], s[4:5], 2
	s_add_u32 s18, s23, s4
	s_addc_u32 s19, s24, s5
	s_add_i32 s8, s12, 2
	s_lshl_b32 s4, s8, 1
	s_ashr_i32 s5, s4, 31
	s_lshl_b64 s[4:5], s[4:5], 2
	s_add_u32 s16, s23, s4
	s_addc_u32 s17, s24, s5
	s_add_i32 s4, s12, 3
	s_lshl_b32 s14, s4, 1
	s_ashr_i32 s15, s14, 31
	s_lshl_b64 s[14:15], s[14:15], 2
	v_ashrrev_i32_e32 v85, 31, v84
	s_add_u32 s14, s23, s14
	v_lshlrev_b64 v[146:147], 3, v[84:85]
	v_readlane_b32 s26, v252, 17
	s_addc_u32 s15, s24, s15
	v_lshl_add_u64 v[42:43], s[0:1], 0, v[146:147]
	v_readlane_b32 s27, v252, 18
	s_ashr_i32 s13, s12, 31
	s_lshl_b64 s[20:21], s[12:13], 12
	v_lshl_add_u64 v[40:41], v[84:85], 4, s[26:27]
	v_lshl_add_u64 v[136:137], v[40:41], 0, s[20:21]
	s_ashr_i32 s11, s10, 31
	s_ashr_i32 s9, s8, 31
	s_ashr_i32 s5, s4, 31
	v_lshl_add_u64 v[146:147], s[2:3], 0, v[146:147]
	s_waitcnt vmcnt(0)
	v_ashrrev_i32_e32 v19, 31, v16
	v_mov_b32_e32 v18, v16
	v_ashrrev_i32_e32 v21, 31, v17
	v_mov_b32_e32 v20, v17
	v_lshlrev_b64 v[16:17], 11, v[20:21]
	v_lshlrev_b64 v[18:19], 11, v[18:19]
	v_lshl_add_u64 v[18:19], v[42:43], 0, v[18:19]
	v_lshl_add_u64 v[16:17], v[42:43], 0, v[16:17]
	global_load_dwordx2 v[158:159], v[18:19], off nt
	global_load_dwordx2 v[156:157], v[16:17], off nt
	global_load_dwordx4 v[78:81], v[136:137], off
	global_load_dwordx2 v[154:155], v[18:19], off offset:512 nt
	global_load_dwordx2 v[152:153], v[16:17], off offset:512 nt
	global_load_dwordx4 v[74:77], v[136:137], off offset:1024
	global_load_dwordx2 v[150:151], v[18:19], off offset:1024 nt
	global_load_dwordx2 v[148:149], v[16:17], off offset:1024 nt
	global_load_dwordx4 v[70:73], v[136:137], off offset:2048
	global_load_dwordx2 v[144:145], v[18:19], off offset:1536 nt
	global_load_dwordx2 v[142:143], v[16:17], off offset:1536 nt
	global_load_dwordx4 v[66:69], v[136:137], off offset:3072
	s_nop 0
	global_load_dwordx2 v[16:17], v65, s[18:19]
	s_lshl_b64 s[18:19], s[10:11], 12
	v_lshl_add_u64 v[102:103], v[40:41], 0, s[18:19]
	s_waitcnt vmcnt(12)
	v_lshlrev_b32_e32 v160, 16, v158
	v_and_b32_e32 v161, 0xffff0000, v158
	s_waitcnt vmcnt(11)
	v_lshlrev_b32_e32 v162, 16, v156
	v_and_b32_e32 v163, 0xffff0000, v156
	v_lshlrev_b32_e32 v158, 16, v159
	v_and_b32_e32 v159, 0xffff0000, v159
	v_lshlrev_b32_e32 v156, 16, v157
	v_and_b32_e32 v157, 0xffff0000, v157
	v_pk_add_f32 v[156:157], v[158:159], v[156:157]
	s_waitcnt vmcnt(8)
	v_lshlrev_b32_e32 v159, 16, v153
	v_pk_add_f32 v[80:81], v[80:81], v[156:157]
	v_lshlrev_b32_e32 v157, 16, v155
	s_waitcnt vmcnt(0)
	v_ashrrev_i32_e32 v19, 31, v16
	v_mov_b32_e32 v18, v16
	v_ashrrev_i32_e32 v21, 31, v17
	v_mov_b32_e32 v20, v17
	v_lshlrev_b64 v[16:17], 11, v[20:21]
	v_lshlrev_b64 v[18:19], 11, v[18:19]
	v_lshl_add_u64 v[18:19], v[42:43], 0, v[18:19]
	v_lshl_add_u64 v[16:17], v[42:43], 0, v[16:17]
	global_load_dwordx2 v[140:141], v[18:19], off nt
	global_load_dwordx2 v[138:139], v[16:17], off nt
	global_load_dwordx4 v[60:63], v[102:103], off
	global_load_dwordx2 v[134:135], v[18:19], off offset:512 nt
	global_load_dwordx2 v[132:133], v[16:17], off offset:512 nt
	global_load_dwordx4 v[48:51], v[102:103], off offset:1024
	global_load_dwordx2 v[122:123], v[18:19], off offset:1024 nt
	global_load_dwordx2 v[120:121], v[16:17], off offset:1024 nt
	global_load_dwordx4 v[36:39], v[102:103], off offset:2048
	global_load_dwordx2 v[110:111], v[18:19], off offset:1536 nt
	global_load_dwordx2 v[108:109], v[16:17], off offset:1536 nt
	global_load_dwordx4 v[32:35], v[102:103], off offset:3072
	s_nop 0
	global_load_dwordx2 v[16:17], v65, s[16:17]
	s_lshl_b64 s[16:17], s[8:9], 12
	v_lshl_add_u64 v[86:87], v[40:41], 0, s[16:17]
	v_lshlrev_b32_e32 v156, 16, v154
	v_lshlrev_b32_e32 v158, 16, v152
	v_pk_add_f32 v[156:157], v[156:157], v[158:159]
	v_mov_b32_e32 v158, v74
	v_mov_b32_e32 v159, v76
	v_and_b32_e32 v155, 0xffff0000, v155
	v_and_b32_e32 v154, 0xffff0000, v154
	v_and_b32_e32 v153, 0xffff0000, v153
	v_and_b32_e32 v152, 0xffff0000, v152
	v_pk_add_f32 v[156:157], v[158:159], v[156:157]
	v_pk_add_f32 v[152:153], v[154:155], v[152:153]
	v_lshlrev_b32_e32 v154, 16, v150
	v_and_b32_e32 v155, 0xffff0000, v150
	v_lshlrev_b32_e32 v158, 16, v148
	v_and_b32_e32 v159, 0xffff0000, v148
	v_lshlrev_b32_e32 v150, 16, v151
	v_and_b32_e32 v151, 0xffff0000, v151
	v_lshlrev_b32_e32 v148, 16, v149
	v_and_b32_e32 v149, 0xffff0000, v149
	v_pk_add_f32 v[148:149], v[150:151], v[148:149]
	v_mov_b32_e32 v76, v75
	v_pk_add_f32 v[72:73], v[72:73], v[148:149]
	v_lshlrev_b32_e32 v148, 16, v144
	v_and_b32_e32 v149, 0xffff0000, v144
	v_lshlrev_b32_e32 v150, 16, v142
	v_and_b32_e32 v151, 0xffff0000, v142
	v_lshlrev_b32_e32 v144, 16, v145
	v_and_b32_e32 v145, 0xffff0000, v145
	v_lshlrev_b32_e32 v142, 16, v143
	v_and_b32_e32 v143, 0xffff0000, v143
	v_pk_add_f32 v[160:161], v[160:161], v[162:163]
	v_pk_add_f32 v[152:153], v[76:77], v[152:153]
	v_pk_add_f32 v[154:155], v[154:155], v[158:159]
	v_pk_add_f32 v[148:149], v[148:149], v[150:151]
	v_pk_add_f32 v[142:143], v[144:145], v[142:143]
	v_pk_add_f32 v[78:79], v[78:79], v[160:161]
	v_mov_b32_e32 v74, v156
	v_mov_b32_e32 v75, v152
	v_mov_b32_e32 v76, v157
	v_mov_b32_e32 v77, v153
	v_pk_add_f32 v[70:71], v[70:71], v[154:155]
	v_pk_add_f32 v[66:67], v[66:67], v[148:149]
	v_pk_add_f32 v[68:69], v[68:69], v[142:143]
	s_waitcnt vmcnt(0)
; DI unsigned pk2(float lo, float hi) { f32x2 v = {lo, hi}; return __builtin_bit_cast(unsigned, __builtin_convertvector(v, bf16v2)); }
; DI float bflo(unsigned w) { return __uint_as_float(w << 16); }
; DI float bfhi(unsigned w) { return __uint_as_float(w & 0xffff0000u); }
;     DI float* outp() const { return (float*)out_g; }
;     ...
;         for (int e = 0; e < 4; ++e) { const u32x2* y0 = (const u32x2*)(YE + (size_t)r0[e] * DM) + lane; const u32x2* y1 = (const u32x2*)(YE + (size_t)r1[e] * DM) + lane; const f32x4* xr = (const f32x4*)(F.outp() + (size_t)(tbase + e) * DM) + lane;
; #pragma unroll
;             for (int j = 0; j < 4; ++j) { ya[e][j] = __builtin_nontemporal_load(y0 + 64 * j); yb[e][j] = __builtin_nontemporal_load(y1 + 64 * j); xv[e][j] = xr[64 * j]; } }
; #pragma unroll
;         for (int e = 0; e < 4; ++e) { const int t = tbase + e; f32x4* xr = (f32x4*)(xout + (size_t)t * DM) + lane; float s = 0.f;
; #pragma unroll
;             for (int j = 0; j < 4; ++j) { f32x4 v = xv[e][j]; const u32x2 a = ya[e][j], b = yb[e][j];
;                 v.x += bflo(a.x) + bflo(b.x); v.y += bfhi(a.x) + bfhi(b.x); v.z += bflo(a.y) + bflo(b.y); v.w += bfhi(a.y) + bfhi(b.y);
;                 xv[e][j] = v; xr[64 * j] = v; s += (v.x * v.x + v.y * v.y) + (v.z * v.z + v.w * v.w); }
;             if (l + 1 < NLAYER) {
;                 const float rs = __builtin_amdgcn_rsqf(wave_sum(s) * (1.f / DM) + 1e-6f);
; #pragma unroll
;                 for (int j = 0; j < 4; ++j) { const f32x4 y = xv[e][j] * rs * gv[j]; u32x2 w; w.x = pk2(y.x, y.y); w.y = pk2(y.z, y.w); *((u32x2*)(XN + (size_t)t * DM) + lane + 64 * j) = w; }
	v_ashrrev_i32_e32 v19, 31, v16
	v_mov_b32_e32 v18, v16
	v_ashrrev_i32_e32 v21, 31, v17
	v_mov_b32_e32 v20, v17
	v_lshlrev_b64 v[16:17], 11, v[20:21]
	v_lshlrev_b64 v[18:19], 11, v[18:19]
	v_lshl_add_u64 v[18:19], v[42:43], 0, v[18:19]
	v_lshl_add_u64 v[16:17], v[42:43], 0, v[16:17]
	global_load_dwordx2 v[106:107], v[18:19], off nt
	global_load_dwordx2 v[104:105], v[16:17], off nt
	global_load_dwordx4 v[28:31], v[86:87], off nt
	global_load_dwordx2 v[100:101], v[18:19], off offset:512 nt
	global_load_dwordx2 v[98:99], v[16:17], off offset:512 nt
	global_load_dwordx4 v[24:27], v[86:87], off offset:1024 nt
	global_load_dwordx2 v[96:97], v[18:19], off offset:1024 nt
	global_load_dwordx2 v[94:95], v[16:17], off offset:1024 nt
	global_load_dwordx4 v[20:23], v[86:87], off offset:2048 nt
	global_load_dwordx2 v[92:93], v[18:19], off offset:1536 nt
	global_load_dwordx2 v[90:91], v[16:17], off offset:1536 nt
	s_nop 0
	global_load_dwordx4 v[16:19], v[86:87], off offset:3072 nt
	global_load_dwordx2 v[44:45], v65, s[14:15]
	s_lshl_b64 s[14:15], s[4:5], 12
	v_lshl_add_u64 v[88:89], v[40:41], 0, s[14:15]
	v_readlane_b32 s14, v252, 32
	v_readlane_b32 s15, v252, 33
	s_and_b64 vcc, exec, s[14:15]
	s_waitcnt vmcnt(0)
	v_ashrrev_i32_e32 v47, 31, v44
	v_mov_b32_e32 v46, v44
	v_ashrrev_i32_e32 v53, 31, v45
	v_mov_b32_e32 v52, v45
	v_lshlrev_b64 v[44:45], 11, v[52:53]
	v_lshlrev_b64 v[46:47], 11, v[46:47]
	v_lshl_add_u64 v[46:47], v[42:43], 0, v[46:47]
	v_lshl_add_u64 v[44:45], v[42:43], 0, v[44:45]
	global_load_dwordx2 v[114:115], v[46:47], off nt
	global_load_dwordx2 v[112:113], v[44:45], off nt
	global_load_dwordx4 v[56:59], v[88:89], off nt
	global_load_dwordx2 v[130:131], v[46:47], off offset:512 nt
	global_load_dwordx2 v[128:129], v[44:45], off offset:512 nt
	global_load_dwordx4 v[40:43], v[88:89], off offset:1024 nt
	global_load_dwordx2 v[118:119], v[46:47], off offset:1024 nt
	global_load_dwordx2 v[116:117], v[44:45], off offset:1024 nt
	global_load_dwordx4 v[52:55], v[88:89], off offset:2048 nt
	global_load_dwordx2 v[126:127], v[46:47], off offset:1536 nt
	global_load_dwordx2 v[124:125], v[44:45], off offset:1536 nt
	s_nop 0
	global_load_dwordx4 v[44:47], v[88:89], off offset:3072 nt
	s_nop 0
	global_store_dwordx4 v[136:137], v[78:81], off nt
	global_store_dwordx4 v[136:137], v[74:77], off offset:1024 nt
	global_store_dwordx4 v[136:137], v[70:73], off offset:2048 nt
	global_store_dwordx4 v[136:137], v[66:69], off offset:3072 nt
	s_cbranch_vccnz .LBB0_3081
	v_mul_f32_e32 v64, v79, v79
	v_pk_fma_f32 v[136:137], v[78:79], v[78:79], v[64:65] op_sel_hi:[1,1,0]
	v_mul_f32_e32 v64, v81, v81
	v_pk_fma_f32 v[142:143], v[80:81], v[80:81], v[64:65] op_sel_hi:[1,1,0]
	v_pk_mul_f32 v[144:145], v[152:153], v[152:153]
	v_mul_f32_e32 v64, v71, v71
	v_pk_fma_f32 v[144:145], v[156:157], v[156:157], v[144:145]
	v_pk_fma_f32 v[148:149], v[70:71], v[70:71], v[64:65] op_sel_hi:[1,1,0]
	v_mul_f32_e32 v64, v73, v73
	v_pk_add_f32 v[144:145], v[144:145], v[144:145] op_sel:[0,1] op_sel_hi:[1,0]
	v_pk_fma_f32 v[150:151], v[72:73], v[72:73], v[64:65] op_sel_hi:[1,1,0]
	v_pk_mul_f32 v[152:153], v[66:67], v[66:67]
	v_pk_mul_f32 v[154:155], v[68:69], v[68:69]
	v_pk_add_f32 v[136:137], v[136:137], v[142:143]
	v_mov_b32_e32 v145, v153
	v_mov_b32_e32 v137, v152
	v_mov_b32_e32 v149, v154
	v_mov_b32_e32 v151, v155
	v_pk_add_f32 v[136:137], v[136:137], v[144:145]
	v_pk_add_f32 v[142:143], v[148:149], v[150:151]
	s_lshl_b64 s[12:13], s[12:13], 10
	v_pk_add_f32 v[136:137], v[136:137], v[142:143]
	s_nop 0
	v_add_f32_e32 v64, v136, v137
	s_nop 1
	v_add_f32_dpp v64, v64, v64 quad_perm:[1,0,3,2] row_mask:0xf bank_mask:0xf bound_ctrl:1
	s_nop 1
	v_add_f32_dpp v64, v64, v64 quad_perm:[2,3,0,1] row_mask:0xf bank_mask:0xf bound_ctrl:1
	s_nop 1
	v_add_f32_dpp v64, v64, v64 row_half_mirror row_mask:0xf bank_mask:0xf bound_ctrl:1
	s_nop 1
	v_add_f32_dpp v64, v64, v64 row_mirror row_mask:0xf bank_mask:0xf bound_ctrl:1
	s_nop 0
	v_readlane_b32 s16, v64, 16
	v_readlane_b32 s17, v64, 48
	v_readlane_b32 s14, v64, 0
	v_readlane_b32 s15, v64, 32
	v_mov_b32_e32 v136, s16
	v_mov_b32_e32 v137, s17
	v_pk_add_f32 v[136:137], s[14:15], v[136:137]
	s_nop 0
	v_add_f32_e32 v64, v136, v137
	v_fmamk_f32 v64, v64, 0x3a800000, v224
	v_rsq_f32_e32 v64, v64
	v_lshl_add_u64 v[136:137], s[12:13], 1, v[146:147]
	v_pk_mul_f32 v[78:79], v[78:79], v[64:65] op_sel_hi:[1,0]
	v_pk_mul_f32 v[80:81], v[80:81], v[64:65] op_sel_hi:[1,0]
	v_pk_mul_f32 v[74:75], v[74:75], v[64:65] op_sel_hi:[1,0]
	v_pk_mul_f32 v[76:77], v[76:77], v[64:65] op_sel_hi:[1,0]
	v_pk_mul_f32 v[70:71], v[70:71], v[64:65] op_sel_hi:[1,0]
	v_pk_mul_f32 v[72:73], v[72:73], v[64:65] op_sel_hi:[1,0]
	v_pk_mul_f32 v[66:67], v[66:67], v[64:65] op_sel_hi:[1,0]
	v_pk_mul_f32 v[68:69], v[68:69], v[64:65] op_sel_hi:[1,0]
	v_pk_mul_f32 v[80:81], v[10:11], v[80:81]
	v_pk_mul_f32 v[78:79], v[8:9], v[78:79]
	v_pk_mul_f32 v[76:77], v[2:3], v[76:77]
	v_pk_mul_f32 v[74:75], v[0:1], v[74:75]
	v_pk_mul_f32 v[72:73], v[6:7], v[72:73]
	v_pk_mul_f32 v[70:71], v[4:5], v[70:71]
	v_pk_mul_f32 v[68:69], v[14:15], v[68:69]
	v_pk_mul_f32 v[66:67], v[12:13], v[66:67]
	v_cvt_pk_bf16_f32 v78, v78, v79
	v_cvt_pk_bf16_f32 v79, v80, v81
	v_cvt_pk_bf16_f32 v74, v74, v75
	v_cvt_pk_bf16_f32 v75, v76, v77
	v_cvt_pk_bf16_f32 v70, v70, v71
	v_cvt_pk_bf16_f32 v71, v72, v73
	v_cvt_pk_bf16_f32 v66, v66, v67
	v_cvt_pk_bf16_f32 v67, v68, v69
	global_store_dwordx2 v[136:137], v[78:79], off
	global_store_dwordx2 v[136:137], v[74:75], off offset:512
	global_store_dwordx2 v[136:137], v[70:71], off offset:1024
	global_store_dwordx2 v[136:137], v[66:67], off offset:1536
; DI unsigned pk2(float lo, float hi) { f32x2 v = {lo, hi}; return __builtin_bit_cast(unsigned, __builtin_convertvector(v, bf16v2)); }
; DI float bflo(unsigned w) { return __uint_as_float(w << 16); }
; DI float bfhi(unsigned w) { return __uint_as_float(w & 0xffff0000u); }
;     ...
;         for (int e = 0; e < 4; ++e) { const int t = tbase + e; f32x4* xr = (f32x4*)(xout + (size_t)t * DM) + lane; float s = 0.f;
; #pragma unroll
;             for (int j = 0; j < 4; ++j) { f32x4 v = xv[e][j]; const u32x2 a = ya[e][j], b = yb[e][j];
;                 v.x += bflo(a.x) + bflo(b.x); v.y += bfhi(a.x) + bfhi(b.x); v.z += bflo(a.y) + bflo(b.y); v.w += bfhi(a.y) + bfhi(b.y);
;                 xv[e][j] = v; xr[64 * j] = v; s += (v.x * v.x + v.y * v.y) + (v.z * v.z + v.w * v.w); }
;             if (l + 1 < NLAYER) {
;                 const float rs = __builtin_amdgcn_rsqf(wave_sum(s) * (1.f / DM) + 1e-6f);
; #pragma unroll
;                 for (int j = 0; j < 4; ++j) { const f32x4 y = xv[e][j] * rs * gv[j]; u32x2 w; w.x = pk2(y.x, y.y); w.y = pk2(y.z, y.w); *((u32x2*)(XN + (size_t)t * DM) + lane + 64 * j) = w; }
.LBB0_3081:
	s_nop 0
	v_lshlrev_b32_e32 v66, 16, v140
	v_and_b32_e32 v67, 0xffff0000, v140
	v_lshlrev_b32_e32 v68, 16, v138
	v_and_b32_e32 v69, 0xffff0000, v138
	v_pk_add_f32 v[66:67], v[66:67], v[68:69]
	v_lshlrev_b32_e32 v68, 16, v139
	v_pk_add_f32 v[60:61], v[60:61], v[66:67]
	v_lshlrev_b32_e32 v66, 16, v141
	v_and_b32_e32 v67, 0xffff0000, v141
	v_and_b32_e32 v69, 0xffff0000, v139
	v_pk_add_f32 v[66:67], v[66:67], v[68:69]
	v_lshlrev_b32_e32 v69, 16, v133
	v_pk_add_f32 v[62:63], v[62:63], v[66:67]
	v_lshlrev_b32_e32 v67, 16, v135
	v_lshlrev_b32_e32 v66, 16, v134
	v_lshlrev_b32_e32 v68, 16, v132
	v_pk_add_f32 v[66:67], v[66:67], v[68:69]
	v_mov_b32_e32 v68, v48
	v_mov_b32_e32 v69, v50
	v_pk_add_f32 v[66:67], v[68:69], v[66:67]
	v_and_b32_e32 v69, 0xffff0000, v135
	v_and_b32_e32 v68, 0xffff0000, v134
	v_and_b32_e32 v71, 0xffff0000, v133
	v_and_b32_e32 v70, 0xffff0000, v132
	v_pk_add_f32 v[68:69], v[68:69], v[70:71]
	v_lshlrev_b32_e32 v70, 16, v122
	v_and_b32_e32 v71, 0xffff0000, v122
	v_lshlrev_b32_e32 v72, 16, v120
	v_and_b32_e32 v73, 0xffff0000, v120
	v_pk_add_f32 v[70:71], v[70:71], v[72:73]
	v_lshlrev_b32_e32 v72, 16, v121
	v_pk_add_f32 v[36:37], v[36:37], v[70:71]
	v_lshlrev_b32_e32 v70, 16, v123
	v_and_b32_e32 v71, 0xffff0000, v123
	v_and_b32_e32 v73, 0xffff0000, v121
	v_pk_add_f32 v[70:71], v[70:71], v[72:73]
	v_lshlrev_b32_e32 v72, 16, v108
	v_pk_add_f32 v[38:39], v[38:39], v[70:71]
	v_lshlrev_b32_e32 v70, 16, v110
	v_and_b32_e32 v71, 0xffff0000, v110
	v_and_b32_e32 v73, 0xffff0000, v108
	v_pk_add_f32 v[70:71], v[70:71], v[72:73]
	v_mov_b32_e32 v50, v49
	v_pk_add_f32 v[32:33], v[32:33], v[70:71]
	v_lshlrev_b32_e32 v70, 16, v111
	v_and_b32_e32 v71, 0xffff0000, v111
	v_lshlrev_b32_e32 v72, 16, v109
	v_and_b32_e32 v73, 0xffff0000, v109
	v_readlane_b32 s12, v252, 32
	v_pk_add_f32 v[68:69], v[50:51], v[68:69]
	v_pk_add_f32 v[70:71], v[70:71], v[72:73]
	v_readlane_b32 s13, v252, 33
	v_mov_b32_e32 v48, v66
	v_mov_b32_e32 v49, v68
	v_mov_b32_e32 v50, v67
	v_mov_b32_e32 v51, v69
	v_pk_add_f32 v[34:35], v[34:35], v[70:71]
	s_and_b64 vcc, exec, s[12:13]
	global_store_dwordx4 v[102:103], v[60:63], off nt
	global_store_dwordx4 v[102:103], v[48:51], off offset:1024 nt
	global_store_dwordx4 v[102:103], v[36:39], off offset:2048 nt
	global_store_dwordx4 v[102:103], v[32:35], off offset:3072 nt
	s_cbranch_vccnz .LBB0_3083
	v_mul_f32_e32 v64, v61, v61
	v_pk_fma_f32 v[70:71], v[60:61], v[60:61], v[64:65] op_sel_hi:[1,1,0]
	v_mul_f32_e32 v64, v63, v63
	v_pk_fma_f32 v[72:73], v[62:63], v[62:63], v[64:65] op_sel_hi:[1,1,0]
	v_pk_mul_f32 v[68:69], v[68:69], v[68:69]
	v_mul_f32_e32 v64, v37, v37
	v_pk_fma_f32 v[66:67], v[66:67], v[66:67], v[68:69]
	v_pk_fma_f32 v[68:69], v[36:37], v[36:37], v[64:65] op_sel_hi:[1,1,0]
	v_mul_f32_e32 v64, v39, v39
	v_pk_add_f32 v[66:67], v[66:67], v[66:67] op_sel:[0,1] op_sel_hi:[1,0]
	v_pk_fma_f32 v[74:75], v[38:39], v[38:39], v[64:65] op_sel_hi:[1,1,0]
	v_pk_mul_f32 v[76:77], v[32:33], v[32:33]
	v_pk_mul_f32 v[78:79], v[34:35], v[34:35]
	v_pk_add_f32 v[70:71], v[70:71], v[72:73]
	v_mov_b32_e32 v67, v77
	v_mov_b32_e32 v71, v76
	v_mov_b32_e32 v69, v78
	v_mov_b32_e32 v75, v79
	v_pk_add_f32 v[66:67], v[70:71], v[66:67]
	v_pk_add_f32 v[68:69], v[68:69], v[74:75]
	s_lshl_b64 s[10:11], s[10:11], 11
	v_pk_add_f32 v[66:67], v[66:67], v[68:69]
	s_nop 0
	v_add_f32_e32 v64, v66, v67
	s_nop 1
	v_add_f32_dpp v64, v64, v64 quad_perm:[1,0,3,2] row_mask:0xf bank_mask:0xf bound_ctrl:1
	s_nop 1
	v_add_f32_dpp v64, v64, v64 quad_perm:[2,3,0,1] row_mask:0xf bank_mask:0xf bound_ctrl:1
	s_nop 1
	v_add_f32_dpp v64, v64, v64 row_half_mirror row_mask:0xf bank_mask:0xf bound_ctrl:1
	s_nop 1
	v_add_f32_dpp v64, v64, v64 row_mirror row_mask:0xf bank_mask:0xf bound_ctrl:1
	s_nop 0
	v_readlane_b32 s14, v64, 16
	v_readlane_b32 s15, v64, 48
	v_readlane_b32 s12, v64, 0
	v_readlane_b32 s13, v64, 32
	v_mov_b32_e32 v66, s14
	v_mov_b32_e32 v67, s15
	v_pk_add_f32 v[66:67], s[12:13], v[66:67]
	s_nop 0
	v_add_f32_e32 v64, v66, v67
	v_fmamk_f32 v64, v64, 0x3a800000, v224
	v_rsq_f32_e32 v64, v64
	v_lshl_add_u64 v[66:67], v[146:147], 0, s[10:11]
	v_pk_mul_f32 v[60:61], v[60:61], v[64:65] op_sel_hi:[1,0]
	v_pk_mul_f32 v[62:63], v[62:63], v[64:65] op_sel_hi:[1,0]
	v_pk_mul_f32 v[48:49], v[48:49], v[64:65] op_sel_hi:[1,0]
	v_pk_mul_f32 v[50:51], v[50:51], v[64:65] op_sel_hi:[1,0]
	v_pk_mul_f32 v[36:37], v[36:37], v[64:65] op_sel_hi:[1,0]
	v_pk_mul_f32 v[38:39], v[38:39], v[64:65] op_sel_hi:[1,0]
	v_pk_mul_f32 v[32:33], v[32:33], v[64:65] op_sel_hi:[1,0]
	v_pk_mul_f32 v[34:35], v[34:35], v[64:65] op_sel_hi:[1,0]
	v_pk_mul_f32 v[62:63], v[10:11], v[62:63]
	v_pk_mul_f32 v[60:61], v[8:9], v[60:61]
	v_pk_mul_f32 v[50:51], v[2:3], v[50:51]
	v_pk_mul_f32 v[48:49], v[0:1], v[48:49]
	v_pk_mul_f32 v[38:39], v[6:7], v[38:39]
	v_pk_mul_f32 v[36:37], v[4:5], v[36:37]
	v_pk_mul_f32 v[34:35], v[14:15], v[34:35]
	v_pk_mul_f32 v[32:33], v[12:13], v[32:33]
	v_cvt_pk_bf16_f32 v60, v60, v61
	v_cvt_pk_bf16_f32 v61, v62, v63
	v_cvt_pk_bf16_f32 v48, v48, v49
	v_cvt_pk_bf16_f32 v49, v50, v51
	v_cvt_pk_bf16_f32 v36, v36, v37
	v_cvt_pk_bf16_f32 v37, v38, v39
	v_cvt_pk_bf16_f32 v32, v32, v33
	v_cvt_pk_bf16_f32 v33, v34, v35
	global_store_dwordx2 v[66:67], v[60:61], off
	global_store_dwordx2 v[66:67], v[48:49], off offset:512
	global_store_dwordx2 v[66:67], v[36:37], off offset:1024
	global_store_dwordx2 v[66:67], v[32:33], off offset:1536
; DI unsigned pk2(float lo, float hi) { f32x2 v = {lo, hi}; return __builtin_bit_cast(unsigned, __builtin_convertvector(v, bf16v2)); }
; DI float bflo(unsigned w) { return __uint_as_float(w << 16); }
; DI float bfhi(unsigned w) { return __uint_as_float(w & 0xffff0000u); }
;     ...
;         for (int e = 0; e < 4; ++e) { const int t = tbase + e; f32x4* xr = (f32x4*)(xout + (size_t)t * DM) + lane; float s = 0.f;
; #pragma unroll
;             for (int j = 0; j < 4; ++j) { f32x4 v = xv[e][j]; const u32x2 a = ya[e][j], b = yb[e][j];
;                 v.x += bflo(a.x) + bflo(b.x); v.y += bfhi(a.x) + bfhi(b.x); v.z += bflo(a.y) + bflo(b.y); v.w += bfhi(a.y) + bfhi(b.y);
;                 xv[e][j] = v; xr[64 * j] = v; s += (v.x * v.x + v.y * v.y) + (v.z * v.z + v.w * v.w); }
;             if (l + 1 < NLAYER) {
;                 const float rs = __builtin_amdgcn_rsqf(wave_sum(s) * (1.f / DM) + 1e-6f);
; #pragma unroll
;                 for (int j = 0; j < 4; ++j) { const f32x4 y = xv[e][j] * rs * gv[j]; u32x2 w; w.x = pk2(y.x, y.y); w.y = pk2(y.z, y.w); *((u32x2*)(XN + (size_t)t * DM) + lane + 64 * j) = w; }
.LBB0_3083:
	s_nop 0
	v_lshlrev_b32_e32 v32, 16, v106
	v_and_b32_e32 v33, 0xffff0000, v106
	v_lshlrev_b32_e32 v34, 16, v104
	v_and_b32_e32 v35, 0xffff0000, v104
	v_pk_add_f32 v[32:33], v[32:33], v[34:35]
	v_lshlrev_b32_e32 v34, 16, v105
	v_pk_add_f32 v[28:29], v[28:29], v[32:33]
	v_lshlrev_b32_e32 v32, 16, v107
	v_and_b32_e32 v33, 0xffff0000, v107
	v_and_b32_e32 v35, 0xffff0000, v105
	v_pk_add_f32 v[32:33], v[32:33], v[34:35]
	v_lshlrev_b32_e32 v35, 16, v99
	v_pk_add_f32 v[30:31], v[30:31], v[32:33]
	v_lshlrev_b32_e32 v33, 16, v101
	v_lshlrev_b32_e32 v32, 16, v100
	v_lshlrev_b32_e32 v34, 16, v98
	v_pk_add_f32 v[32:33], v[32:33], v[34:35]
	v_mov_b32_e32 v34, v24
	v_mov_b32_e32 v35, v26
	v_pk_add_f32 v[32:33], v[34:35], v[32:33]
	v_and_b32_e32 v35, 0xffff0000, v101
	v_and_b32_e32 v34, 0xffff0000, v100
	v_and_b32_e32 v37, 0xffff0000, v99
	v_and_b32_e32 v36, 0xffff0000, v98
	v_pk_add_f32 v[34:35], v[34:35], v[36:37]
	v_lshlrev_b32_e32 v36, 16, v96
	v_and_b32_e32 v37, 0xffff0000, v96
	v_lshlrev_b32_e32 v38, 16, v94
	v_and_b32_e32 v39, 0xffff0000, v94
	v_pk_add_f32 v[36:37], v[36:37], v[38:39]
	v_lshlrev_b32_e32 v38, 16, v95
	v_pk_add_f32 v[20:21], v[20:21], v[36:37]
	v_lshlrev_b32_e32 v36, 16, v97
	v_and_b32_e32 v37, 0xffff0000, v97
	v_and_b32_e32 v39, 0xffff0000, v95
	v_pk_add_f32 v[36:37], v[36:37], v[38:39]
	v_lshlrev_b32_e32 v38, 16, v90
	v_pk_add_f32 v[22:23], v[22:23], v[36:37]
	v_lshlrev_b32_e32 v36, 16, v92
	v_and_b32_e32 v37, 0xffff0000, v92
	v_and_b32_e32 v39, 0xffff0000, v90
	v_pk_add_f32 v[36:37], v[36:37], v[38:39]
	v_mov_b32_e32 v26, v25
	v_pk_add_f32 v[16:17], v[16:17], v[36:37]
	v_lshlrev_b32_e32 v36, 16, v93
	v_and_b32_e32 v37, 0xffff0000, v93
	v_lshlrev_b32_e32 v38, 16, v91
	v_and_b32_e32 v39, 0xffff0000, v91
	v_readlane_b32 s10, v252, 32
	v_pk_add_f32 v[34:35], v[26:27], v[34:35]
	v_pk_add_f32 v[36:37], v[36:37], v[38:39]
	v_readlane_b32 s11, v252, 33
	v_mov_b32_e32 v24, v32
	v_mov_b32_e32 v25, v34
	v_mov_b32_e32 v26, v33
	v_mov_b32_e32 v27, v35
	v_pk_add_f32 v[18:19], v[18:19], v[36:37]
	s_and_b64 vcc, exec, s[10:11]
	global_store_dwordx4 v[86:87], v[28:31], off nt
	global_store_dwordx4 v[86:87], v[24:27], off offset:1024 nt
	global_store_dwordx4 v[86:87], v[20:23], off offset:2048 nt
	global_store_dwordx4 v[86:87], v[16:19], off offset:3072 nt
	s_cbranch_vccnz .LBB0_3085
	v_mul_f32_e32 v36, v29, v29
	v_mul_f32_e32 v38, v31, v31
	v_pk_mul_f32 v[34:35], v[34:35], v[34:35]
	v_pk_fma_f32 v[36:37], v[28:29], v[28:29], v[36:37] op_sel_hi:[1,1,0]
	v_pk_fma_f32 v[38:39], v[30:31], v[30:31], v[38:39] op_sel_hi:[1,1,0]
	v_pk_fma_f32 v[32:33], v[32:33], v[32:33], v[34:35]
	v_mul_f32_e32 v34, v21, v21
	v_mul_f32_e32 v48, v23, v23
	v_pk_add_f32 v[32:33], v[32:33], v[32:33] op_sel:[0,1] op_sel_hi:[1,0]
	v_pk_fma_f32 v[34:35], v[20:21], v[20:21], v[34:35] op_sel_hi:[1,1,0]
	v_pk_fma_f32 v[48:49], v[22:23], v[22:23], v[48:49] op_sel_hi:[1,1,0]
	v_pk_mul_f32 v[50:51], v[16:17], v[16:17]
	v_pk_mul_f32 v[60:61], v[18:19], v[18:19]
	v_pk_add_f32 v[36:37], v[36:37], v[38:39]
	v_mov_b32_e32 v33, v51
	v_mov_b32_e32 v37, v50
	v_mov_b32_e32 v35, v60
	v_mov_b32_e32 v49, v61
	v_pk_add_f32 v[32:33], v[36:37], v[32:33]
	v_pk_add_f32 v[34:35], v[34:35], v[48:49]
	s_lshl_b64 s[8:9], s[8:9], 11
	v_pk_add_f32 v[32:33], v[32:33], v[34:35]
	v_lshl_add_u64 v[34:35], v[146:147], 0, s[8:9]
	v_add_f32_e32 v32, v32, v33
	s_nop 1
	v_add_f32_dpp v32, v32, v32 quad_perm:[1,0,3,2] row_mask:0xf bank_mask:0xf bound_ctrl:1
	s_nop 1
	v_add_f32_dpp v32, v32, v32 quad_perm:[2,3,0,1] row_mask:0xf bank_mask:0xf bound_ctrl:1
	s_nop 1
	v_add_f32_dpp v32, v32, v32 row_half_mirror row_mask:0xf bank_mask:0xf bound_ctrl:1
	s_nop 1
	v_add_f32_dpp v32, v32, v32 row_mirror row_mask:0xf bank_mask:0xf bound_ctrl:1
	s_nop 0
	v_readlane_b32 s12, v32, 16
	v_readlane_b32 s13, v32, 48
	v_readlane_b32 s10, v32, 0
	v_readlane_b32 s11, v32, 32
	v_mov_b32_e32 v32, s12
	v_mov_b32_e32 v33, s13
	v_pk_add_f32 v[32:33], s[10:11], v[32:33]
	s_nop 0
	v_add_f32_e32 v32, v32, v33
	v_fmamk_f32 v32, v32, 0x3a800000, v224
	v_rsq_f32_e32 v32, v32
	s_nop 0
	v_pk_mul_f32 v[28:29], v[28:29], v[32:33] op_sel_hi:[1,0]
	v_pk_mul_f32 v[30:31], v[30:31], v[32:33] op_sel_hi:[1,0]
	v_pk_mul_f32 v[24:25], v[24:25], v[32:33] op_sel_hi:[1,0]
	v_pk_mul_f32 v[26:27], v[26:27], v[32:33] op_sel_hi:[1,0]
	v_pk_mul_f32 v[20:21], v[20:21], v[32:33] op_sel_hi:[1,0]
	v_pk_mul_f32 v[22:23], v[22:23], v[32:33] op_sel_hi:[1,0]
	v_pk_mul_f32 v[16:17], v[16:17], v[32:33] op_sel_hi:[1,0]
	v_pk_mul_f32 v[18:19], v[18:19], v[32:33] op_sel_hi:[1,0]
	v_pk_mul_f32 v[30:31], v[10:11], v[30:31]
	v_pk_mul_f32 v[28:29], v[8:9], v[28:29]
	v_pk_mul_f32 v[26:27], v[2:3], v[26:27]
	v_pk_mul_f32 v[24:25], v[0:1], v[24:25]
	v_pk_mul_f32 v[22:23], v[6:7], v[22:23]
	v_pk_mul_f32 v[20:21], v[4:5], v[20:21]
	v_pk_mul_f32 v[18:19], v[14:15], v[18:19]
	v_pk_mul_f32 v[16:17], v[12:13], v[16:17]
	v_cvt_pk_bf16_f32 v28, v28, v29
	v_cvt_pk_bf16_f32 v29, v30, v31
	v_cvt_pk_bf16_f32 v24, v24, v25
	v_cvt_pk_bf16_f32 v25, v26, v27
	v_cvt_pk_bf16_f32 v20, v20, v21
	v_cvt_pk_bf16_f32 v21, v22, v23
	v_cvt_pk_bf16_f32 v16, v16, v17
	v_cvt_pk_bf16_f32 v17, v18, v19
	global_store_dwordx2 v[34:35], v[28:29], off
	global_store_dwordx2 v[34:35], v[24:25], off offset:512
	global_store_dwordx2 v[34:35], v[20:21], off offset:1024
	global_store_dwordx2 v[34:35], v[16:17], off offset:1536
; DI unsigned pk2(float lo, float hi) { f32x2 v = {lo, hi}; return __builtin_bit_cast(unsigned, __builtin_convertvector(v, bf16v2)); }
; DI float bflo(unsigned w) { return __uint_as_float(w << 16); }
; DI float bfhi(unsigned w) { return __uint_as_float(w & 0xffff0000u); }
;     ...
;         for (int e = 0; e < 4; ++e) { const int t = tbase + e; f32x4* xr = (f32x4*)(xout + (size_t)t * DM) + lane; float s = 0.f;
; #pragma unroll
;             for (int j = 0; j < 4; ++j) { f32x4 v = xv[e][j]; const u32x2 a = ya[e][j], b = yb[e][j];
;                 v.x += bflo(a.x) + bflo(b.x); v.y += bfhi(a.x) + bfhi(b.x); v.z += bflo(a.y) + bflo(b.y); v.w += bfhi(a.y) + bfhi(b.y);
;                 xv[e][j] = v; xr[64 * j] = v; s += (v.x * v.x + v.y * v.y) + (v.z * v.z + v.w * v.w); }
;             if (l + 1 < NLAYER) {
;                 const float rs = __builtin_amdgcn_rsqf(wave_sum(s) * (1.f / DM) + 1e-6f);
; #pragma unroll
;                 for (int j = 0; j < 4; ++j) { const f32x4 y = xv[e][j] * rs * gv[j]; u32x2 w; w.x = pk2(y.x, y.y); w.y = pk2(y.z, y.w); *((u32x2*)(XN + (size_t)t * DM) + lane + 64 * j) = w; }
.LBB0_3085:
	s_waitcnt vmcnt(23)
	v_lshlrev_b32_e32 v16, 16, v114
	v_and_b32_e32 v17, 0xffff0000, v114
	s_waitcnt vmcnt(22)
	v_lshlrev_b32_e32 v18, 16, v112
	v_and_b32_e32 v19, 0xffff0000, v112
	v_pk_add_f32 v[16:17], v[16:17], v[18:19]
	v_lshlrev_b32_e32 v18, 16, v115
	v_and_b32_e32 v19, 0xffff0000, v115
	v_lshlrev_b32_e32 v20, 16, v113
	v_and_b32_e32 v21, 0xffff0000, v113
	v_pk_add_f32 v[18:19], v[18:19], v[20:21]
	s_waitcnt vmcnt(20)
	v_lshlrev_b32_e32 v21, 16, v131
	v_lshlrev_b32_e32 v20, 16, v130
	s_waitcnt vmcnt(19)
	v_lshlrev_b32_e32 v23, 16, v129
	v_lshlrev_b32_e32 v22, 16, v128
	s_waitcnt vmcnt(17)
	v_lshlrev_b32_e32 v24, 16, v118
	v_and_b32_e32 v25, 0xffff0000, v118
	s_waitcnt vmcnt(16)
	v_lshlrev_b32_e32 v26, 16, v116
	v_and_b32_e32 v27, 0xffff0000, v116
	v_pk_add_f32 v[20:21], v[20:21], v[22:23]
	v_mov_b32_e32 v22, v40
	v_mov_b32_e32 v23, v42
	v_pk_add_f32 v[24:25], v[24:25], v[26:27]
	v_lshlrev_b32_e32 v26, 16, v119
	v_and_b32_e32 v27, 0xffff0000, v119
	v_lshlrev_b32_e32 v28, 16, v117
	v_and_b32_e32 v29, 0xffff0000, v117
	v_pk_add_f32 v[32:33], v[22:23], v[20:21]
	v_and_b32_e32 v21, 0xffff0000, v131
	v_and_b32_e32 v20, 0xffff0000, v130
	v_and_b32_e32 v23, 0xffff0000, v129
	v_and_b32_e32 v22, 0xffff0000, v128
	v_pk_add_f32 v[26:27], v[26:27], v[28:29]
	s_waitcnt vmcnt(14)
	v_lshlrev_b32_e32 v28, 16, v126
	v_and_b32_e32 v29, 0xffff0000, v126
	s_waitcnt vmcnt(13)
	v_lshlrev_b32_e32 v30, 16, v124
	v_and_b32_e32 v31, 0xffff0000, v124
	v_pk_add_f32 v[20:21], v[20:21], v[22:23]
	v_mov_b32_e32 v42, v41
	v_pk_add_f32 v[28:29], v[28:29], v[30:31]
	v_lshlrev_b32_e32 v30, 16, v127
	v_and_b32_e32 v31, 0xffff0000, v127
	v_lshlrev_b32_e32 v36, 16, v125
	v_and_b32_e32 v37, 0xffff0000, v125
	v_readlane_b32 s8, v252, 32
	v_pk_add_f32 v[34:35], v[42:43], v[20:21]
	v_pk_add_f32 v[30:31], v[30:31], v[36:37]
	v_readlane_b32 s9, v252, 33
	v_pk_add_f32 v[16:17], v[56:57], v[16:17]
	v_pk_add_f32 v[18:19], v[58:59], v[18:19]
	v_mov_b32_e32 v20, v32
	v_mov_b32_e32 v21, v34
	v_mov_b32_e32 v22, v33
	v_mov_b32_e32 v23, v35
	v_pk_add_f32 v[24:25], v[52:53], v[24:25]
	v_pk_add_f32 v[26:27], v[54:55], v[26:27]
	s_waitcnt vmcnt(12)
	v_pk_add_f32 v[28:29], v[44:45], v[28:29]
	v_pk_add_f32 v[30:31], v[46:47], v[30:31]
	s_and_b64 vcc, exec, s[8:9]
	global_store_dwordx4 v[88:89], v[16:19], off nt
	global_store_dwordx4 v[88:89], v[20:23], off offset:1024 nt
	global_store_dwordx4 v[88:89], v[24:27], off offset:2048 nt
	global_store_dwordx4 v[88:89], v[28:31], off offset:3072 nt
	s_cbranch_vccnz .LBB0_3078
	v_mul_f32_e32 v36, v17, v17
	v_mul_f32_e32 v38, v19, v19
	v_pk_mul_f32 v[34:35], v[34:35], v[34:35]
	v_pk_fma_f32 v[36:37], v[16:17], v[16:17], v[36:37] op_sel_hi:[1,1,0]
	v_pk_fma_f32 v[38:39], v[18:19], v[18:19], v[38:39] op_sel_hi:[1,1,0]
	v_pk_fma_f32 v[32:33], v[32:33], v[32:33], v[34:35]
	v_mul_f32_e32 v34, v25, v25
	v_mul_f32_e32 v40, v27, v27
	v_pk_add_f32 v[32:33], v[32:33], v[32:33] op_sel:[0,1] op_sel_hi:[1,0]
	v_pk_fma_f32 v[34:35], v[24:25], v[24:25], v[34:35] op_sel_hi:[1,1,0]
	v_pk_fma_f32 v[40:41], v[26:27], v[26:27], v[40:41] op_sel_hi:[1,1,0]
	v_pk_mul_f32 v[42:43], v[28:29], v[28:29]
	v_pk_mul_f32 v[44:45], v[30:31], v[30:31]
	v_pk_add_f32 v[36:37], v[36:37], v[38:39]
	v_mov_b32_e32 v33, v43
	v_mov_b32_e32 v37, v42
	v_mov_b32_e32 v35, v44
	v_mov_b32_e32 v41, v45
	v_pk_add_f32 v[32:33], v[36:37], v[32:33]
	v_pk_add_f32 v[34:35], v[34:35], v[40:41]
	s_lshl_b64 s[4:5], s[4:5], 11
	v_pk_add_f32 v[32:33], v[32:33], v[34:35]
	v_lshl_add_u64 v[34:35], v[146:147], 0, s[4:5]
	v_add_f32_e32 v32, v32, v33
	s_nop 1
	v_add_f32_dpp v32, v32, v32 quad_perm:[1,0,3,2] row_mask:0xf bank_mask:0xf bound_ctrl:1
	s_nop 1
	v_add_f32_dpp v32, v32, v32 quad_perm:[2,3,0,1] row_mask:0xf bank_mask:0xf bound_ctrl:1
	s_nop 1
	v_add_f32_dpp v32, v32, v32 row_half_mirror row_mask:0xf bank_mask:0xf bound_ctrl:1
	s_nop 1
	v_add_f32_dpp v32, v32, v32 row_mirror row_mask:0xf bank_mask:0xf bound_ctrl:1
	s_nop 0
	v_readlane_b32 s10, v32, 16
	v_readlane_b32 s11, v32, 48
	v_readlane_b32 s8, v32, 0
	v_readlane_b32 s9, v32, 32
	v_mov_b32_e32 v32, s10
	v_mov_b32_e32 v33, s11
	v_pk_add_f32 v[32:33], s[8:9], v[32:33]
	s_nop 0
	v_add_f32_e32 v32, v32, v33
	v_fmamk_f32 v32, v32, 0x3a800000, v224
	v_rsq_f32_e32 v32, v32
	s_nop 0
	v_pk_mul_f32 v[16:17], v[16:17], v[32:33] op_sel_hi:[1,0]
	v_pk_mul_f32 v[18:19], v[18:19], v[32:33] op_sel_hi:[1,0]
	v_pk_mul_f32 v[16:17], v[8:9], v[16:17]
	v_pk_mul_f32 v[18:19], v[10:11], v[18:19]
	v_cvt_pk_bf16_f32 v16, v16, v17
	v_cvt_pk_bf16_f32 v17, v18, v19
	global_store_dwordx2 v[34:35], v[16:17], off
	v_pk_mul_f32 v[16:17], v[20:21], v[32:33] op_sel_hi:[1,0]
	v_pk_mul_f32 v[18:19], v[22:23], v[32:33] op_sel_hi:[1,0]
	v_pk_mul_f32 v[16:17], v[0:1], v[16:17]
	v_pk_mul_f32 v[18:19], v[2:3], v[18:19]
	v_cvt_pk_bf16_f32 v16, v16, v17
	v_cvt_pk_bf16_f32 v17, v18, v19
	global_store_dwordx2 v[34:35], v[16:17], off offset:512
	v_pk_mul_f32 v[16:17], v[24:25], v[32:33] op_sel_hi:[1,0]
	v_pk_mul_f32 v[18:19], v[26:27], v[32:33] op_sel_hi:[1,0]
	v_pk_mul_f32 v[16:17], v[4:5], v[16:17]
	v_pk_mul_f32 v[18:19], v[6:7], v[18:19]
	v_cvt_pk_bf16_f32 v16, v16, v17
	v_cvt_pk_bf16_f32 v17, v18, v19
	global_store_dwordx2 v[34:35], v[16:17], off offset:1024
	v_pk_mul_f32 v[16:17], v[28:29], v[32:33] op_sel_hi:[1,0]
	v_pk_mul_f32 v[18:19], v[30:31], v[32:33] op_sel_hi:[1,0]
	v_pk_mul_f32 v[16:17], v[12:13], v[16:17]
	v_pk_mul_f32 v[18:19], v[14:15], v[18:19]
	v_cvt_pk_bf16_f32 v16, v16, v17
	v_cvt_pk_bf16_f32 v17, v18, v19
	global_store_dwordx2 v[34:35], v[16:17], off offset:1536
	s_branch .LBB0_3078
